# P3 attention unit: K-norm/V staging and Q-norm fragments rewritten (8 rows interleaved, DPP row_ror reductions instead of serialized ds_bpermute, v_rsq_f32 instead of IEEE sqrt+div expansions, hoisted
# baseline (speedup 1.0000x reference)
.LBB0_711:
	s_or_b64 exec, exec, s[10:11]
	s_waitcnt vmcnt(0)
	ds_read_b128 v[218:221], v144
	ds_read_b128 v[222:225], v144 offset:16
	ds_read_b128 v[226:229], v200
	ds_read_b128 v[230:233], v200 offset:16
	ds_read_b128 v[234:237], v200 offset:128
	ds_read_b128 v[238:241], v200 offset:144
	ds_read_b128 v[242:245], v200 offset:256
	ds_read_b128 v[246:249], v200 offset:272
	ds_read_b128 v[250:253], v200 offset:384
	ds_read_b128 v[120:123], v200 offset:400
	v_and_b32_e32 v108, 0xffff0000, v2
	v_and_b32_e32 v109, 0xffff0000, v10
	v_and_b32_e32 v110, 0xffff0000, v18
	v_and_b32_e32 v111, 0xffff0000, v26
	v_and_b32_e32 v112, 0xffff0000, v34
	v_and_b32_e32 v113, 0xffff0000, v42
	v_and_b32_e32 v114, 0xffff0000, v52
	v_and_b32_e32 v115, 0xffff0000, v60
	v_mul_f32_e32 v100, v108, v108
	v_mul_f32_e32 v101, v109, v109
	v_mul_f32_e32 v102, v110, v110
	v_mul_f32_e32 v103, v111, v111
	v_mul_f32_e32 v104, v112, v112
	v_mul_f32_e32 v105, v113, v113
	v_mul_f32_e32 v106, v114, v114
	v_mul_f32_e32 v107, v115, v115
	v_lshlrev_b32_e32 v108, 16, v2
	v_lshlrev_b32_e32 v109, 16, v10
	v_lshlrev_b32_e32 v110, 16, v18
	v_lshlrev_b32_e32 v111, 16, v26
	v_lshlrev_b32_e32 v112, 16, v34
	v_lshlrev_b32_e32 v113, 16, v42
	v_lshlrev_b32_e32 v114, 16, v52
	v_lshlrev_b32_e32 v115, 16, v60
	v_fmac_f32_e32 v100, v108, v108
	v_fmac_f32_e32 v101, v109, v109
	v_fmac_f32_e32 v102, v110, v110
	v_fmac_f32_e32 v103, v111, v111
	v_fmac_f32_e32 v104, v112, v112
	v_fmac_f32_e32 v105, v113, v113
	v_fmac_f32_e32 v106, v114, v114
	v_fmac_f32_e32 v107, v115, v115
	v_lshlrev_b32_e32 v108, 16, v3
	v_lshlrev_b32_e32 v109, 16, v11
	v_lshlrev_b32_e32 v110, 16, v19
	v_lshlrev_b32_e32 v111, 16, v27
	v_lshlrev_b32_e32 v112, 16, v35
	v_lshlrev_b32_e32 v113, 16, v43
	v_lshlrev_b32_e32 v114, 16, v53
	v_lshlrev_b32_e32 v115, 16, v61
	v_fmac_f32_e32 v100, v108, v108
	v_fmac_f32_e32 v101, v109, v109
	v_fmac_f32_e32 v102, v110, v110
	v_fmac_f32_e32 v103, v111, v111
	v_fmac_f32_e32 v104, v112, v112
	v_fmac_f32_e32 v105, v113, v113
	v_fmac_f32_e32 v106, v114, v114
	v_fmac_f32_e32 v107, v115, v115
	v_and_b32_e32 v108, 0xffff0000, v3
	v_and_b32_e32 v109, 0xffff0000, v11
	v_and_b32_e32 v110, 0xffff0000, v19
	v_and_b32_e32 v111, 0xffff0000, v27
	v_and_b32_e32 v112, 0xffff0000, v35
	v_and_b32_e32 v113, 0xffff0000, v43
	v_and_b32_e32 v114, 0xffff0000, v53
	v_and_b32_e32 v115, 0xffff0000, v61
	v_fmac_f32_e32 v100, v108, v108
	v_fmac_f32_e32 v101, v109, v109
	v_fmac_f32_e32 v102, v110, v110
	v_fmac_f32_e32 v103, v111, v111
	v_fmac_f32_e32 v104, v112, v112
	v_fmac_f32_e32 v105, v113, v113
	v_fmac_f32_e32 v106, v114, v114
	v_fmac_f32_e32 v107, v115, v115
	v_lshlrev_b32_e32 v108, 16, v4
	v_lshlrev_b32_e32 v109, 16, v12
	v_lshlrev_b32_e32 v110, 16, v20
	v_lshlrev_b32_e32 v111, 16, v28
	v_lshlrev_b32_e32 v112, 16, v36
	v_lshlrev_b32_e32 v113, 16, v44
	v_lshlrev_b32_e32 v114, 16, v54
	v_lshlrev_b32_e32 v115, 16, v62
	v_fmac_f32_e32 v100, v108, v108
	v_fmac_f32_e32 v101, v109, v109
	v_fmac_f32_e32 v102, v110, v110
	v_fmac_f32_e32 v103, v111, v111
	v_fmac_f32_e32 v104, v112, v112
	v_fmac_f32_e32 v105, v113, v113
	v_fmac_f32_e32 v106, v114, v114
	v_fmac_f32_e32 v107, v115, v115
	v_and_b32_e32 v108, 0xffff0000, v4
	v_and_b32_e32 v109, 0xffff0000, v12
	v_and_b32_e32 v110, 0xffff0000, v20
	v_and_b32_e32 v111, 0xffff0000, v28
	v_and_b32_e32 v112, 0xffff0000, v36
	v_and_b32_e32 v113, 0xffff0000, v44
	v_and_b32_e32 v114, 0xffff0000, v54
	v_and_b32_e32 v115, 0xffff0000, v62
	v_fmac_f32_e32 v100, v108, v108
	v_fmac_f32_e32 v101, v109, v109
	v_fmac_f32_e32 v102, v110, v110
	v_fmac_f32_e32 v103, v111, v111
	v_fmac_f32_e32 v104, v112, v112
	v_fmac_f32_e32 v105, v113, v113
	v_fmac_f32_e32 v106, v114, v114
	v_fmac_f32_e32 v107, v115, v115
	v_lshlrev_b32_e32 v108, 16, v5
	v_lshlrev_b32_e32 v109, 16, v13
	v_lshlrev_b32_e32 v110, 16, v21
	v_lshlrev_b32_e32 v111, 16, v29
	v_lshlrev_b32_e32 v112, 16, v37
	v_lshlrev_b32_e32 v113, 16, v45
	v_lshlrev_b32_e32 v114, 16, v55
	v_lshlrev_b32_e32 v115, 16, v63
	v_fmac_f32_e32 v100, v108, v108
	v_fmac_f32_e32 v101, v109, v109
	v_fmac_f32_e32 v102, v110, v110
	v_fmac_f32_e32 v103, v111, v111
	v_fmac_f32_e32 v104, v112, v112
	v_fmac_f32_e32 v105, v113, v113
	v_fmac_f32_e32 v106, v114, v114
	v_fmac_f32_e32 v107, v115, v115
	v_and_b32_e32 v108, 0xffff0000, v5
	v_and_b32_e32 v109, 0xffff0000, v13
	v_and_b32_e32 v110, 0xffff0000, v21
	v_and_b32_e32 v111, 0xffff0000, v29
	v_and_b32_e32 v112, 0xffff0000, v37
	v_and_b32_e32 v113, 0xffff0000, v45
	v_and_b32_e32 v114, 0xffff0000, v55
	v_and_b32_e32 v115, 0xffff0000, v63
	v_fmac_f32_e32 v100, v108, v108
	v_fmac_f32_e32 v101, v109, v109
	v_fmac_f32_e32 v102, v110, v110
	v_fmac_f32_e32 v103, v111, v111
	v_fmac_f32_e32 v104, v112, v112
	v_fmac_f32_e32 v105, v113, v113
	v_fmac_f32_e32 v106, v114, v114
	v_fmac_f32_e32 v107, v115, v115
	v_add_f32_dpp v100, v100, v100 row_ror:8 row_mask:0xf bank_mask:0xf
	v_add_f32_dpp v101, v101, v101 row_ror:8 row_mask:0xf bank_mask:0xf
	v_add_f32_dpp v102, v102, v102 row_ror:8 row_mask:0xf bank_mask:0xf
	v_add_f32_dpp v103, v103, v103 row_ror:8 row_mask:0xf bank_mask:0xf
	v_add_f32_dpp v104, v104, v104 row_ror:8 row_mask:0xf bank_mask:0xf
	v_add_f32_dpp v105, v105, v105 row_ror:8 row_mask:0xf bank_mask:0xf
	v_add_f32_dpp v106, v106, v106 row_ror:8 row_mask:0xf bank_mask:0xf
	v_add_f32_dpp v107, v107, v107 row_ror:8 row_mask:0xf bank_mask:0xf
	v_add_f32_dpp v100, v100, v100 row_ror:4 row_mask:0xf bank_mask:0xf
	v_add_f32_dpp v101, v101, v101 row_ror:4 row_mask:0xf bank_mask:0xf
	v_add_f32_dpp v102, v102, v102 row_ror:4 row_mask:0xf bank_mask:0xf
	v_add_f32_dpp v103, v103, v103 row_ror:4 row_mask:0xf bank_mask:0xf
	v_add_f32_dpp v104, v104, v104 row_ror:4 row_mask:0xf bank_mask:0xf
	v_add_f32_dpp v105, v105, v105 row_ror:4 row_mask:0xf bank_mask:0xf
	v_add_f32_dpp v106, v106, v106 row_ror:4 row_mask:0xf bank_mask:0xf
	v_add_f32_dpp v107, v107, v107 row_ror:4 row_mask:0xf bank_mask:0xf
	v_add_f32_dpp v100, v100, v100 row_ror:2 row_mask:0xf bank_mask:0xf
	v_add_f32_dpp v101, v101, v101 row_ror:2 row_mask:0xf bank_mask:0xf
	v_add_f32_dpp v102, v102, v102 row_ror:2 row_mask:0xf bank_mask:0xf
	v_add_f32_dpp v103, v103, v103 row_ror:2 row_mask:0xf bank_mask:0xf
	v_add_f32_dpp v104, v104, v104 row_ror:2 row_mask:0xf bank_mask:0xf
	v_add_f32_dpp v105, v105, v105 row_ror:2 row_mask:0xf bank_mask:0xf
	v_add_f32_dpp v106, v106, v106 row_ror:2 row_mask:0xf bank_mask:0xf
	v_add_f32_dpp v107, v107, v107 row_ror:2 row_mask:0xf bank_mask:0xf
	v_add_f32_dpp v100, v100, v100 row_ror:1 row_mask:0xf bank_mask:0xf
	v_add_f32_dpp v101, v101, v101 row_ror:1 row_mask:0xf bank_mask:0xf
	v_add_f32_dpp v102, v102, v102 row_ror:1 row_mask:0xf bank_mask:0xf
	v_add_f32_dpp v103, v103, v103 row_ror:1 row_mask:0xf bank_mask:0xf
	v_add_f32_dpp v104, v104, v104 row_ror:1 row_mask:0xf bank_mask:0xf
	v_add_f32_dpp v105, v105, v105 row_ror:1 row_mask:0xf bank_mask:0xf
	v_add_f32_dpp v106, v106, v106 row_ror:1 row_mask:0xf bank_mask:0xf
	v_add_f32_dpp v107, v107, v107 row_ror:1 row_mask:0xf bank_mask:0xf
	v_fmamk_f32 v100, v100, 0x3c000000, v198
	v_fmamk_f32 v101, v101, 0x3c000000, v198
	v_fmamk_f32 v102, v102, 0x3c000000, v198
	v_fmamk_f32 v103, v103, 0x3c000000, v198
	v_fmamk_f32 v104, v104, 0x3c000000, v198
	v_fmamk_f32 v105, v105, 0x3c000000, v198
	v_fmamk_f32 v106, v106, 0x3c000000, v198
	v_fmamk_f32 v107, v107, 0x3c000000, v198
	v_rsq_f32_e32 v100, v100
	v_rsq_f32_e32 v101, v101
	v_rsq_f32_e32 v102, v102
	v_rsq_f32_e32 v103, v103
	v_rsq_f32_e32 v104, v104
	v_rsq_f32_e32 v105, v105
	v_rsq_f32_e32 v106, v106
	v_rsq_f32_e32 v107, v107
	s_waitcnt lgkmcnt(8)
	v_lshlrev_b32_e32 v108, 16, v2
	v_and_b32_e32 v109, 0xffff0000, v2
	v_lshlrev_b32_e32 v110, 16, v3
	v_and_b32_e32 v111, 0xffff0000, v3
	v_lshlrev_b32_e32 v112, 16, v4
	v_and_b32_e32 v113, 0xffff0000, v4
	v_lshlrev_b32_e32 v114, 16, v5
	v_and_b32_e32 v115, 0xffff0000, v5
	v_mul_f32_e32 v108, v100, v108
	v_mul_f32_e32 v109, v100, v109
	v_mul_f32_e32 v110, v100, v110
	v_mul_f32_e32 v111, v100, v111
	v_mul_f32_e32 v112, v100, v112
	v_mul_f32_e32 v113, v100, v113
	v_mul_f32_e32 v114, v100, v114
	v_mul_f32_e32 v115, v100, v115
	v_mul_f32_e32 v108, v218, v108
	v_mul_f32_e32 v109, v219, v109
	v_mul_f32_e32 v110, v220, v110
	v_mul_f32_e32 v111, v221, v111
	v_mul_f32_e32 v112, v222, v112
	v_mul_f32_e32 v113, v223, v113
	v_mul_f32_e32 v114, v224, v114
	v_mul_f32_e32 v115, v225, v115
	v_cvt_pk_bf16_f32 v108, v108, v109
	v_cvt_pk_bf16_f32 v109, v110, v111
	v_cvt_pk_bf16_f32 v110, v112, v113
	v_cvt_pk_bf16_f32 v111, v114, v115
	ds_write_b128 v151, v[108:111]
	ds_write_b128 v152, v[6:9]
	v_lshlrev_b32_e32 v84, 16, v10
	v_and_b32_e32 v85, 0xffff0000, v10
	v_lshlrev_b32_e32 v86, 16, v11
	v_and_b32_e32 v87, 0xffff0000, v11
	v_lshlrev_b32_e32 v88, 16, v12
	v_and_b32_e32 v89, 0xffff0000, v12
	v_lshlrev_b32_e32 v90, 16, v13
	v_and_b32_e32 v91, 0xffff0000, v13
	v_mul_f32_e32 v84, v101, v84
	v_mul_f32_e32 v85, v101, v85
	v_mul_f32_e32 v86, v101, v86
	v_mul_f32_e32 v87, v101, v87
	v_mul_f32_e32 v88, v101, v88
	v_mul_f32_e32 v89, v101, v89
	v_mul_f32_e32 v90, v101, v90
	v_mul_f32_e32 v91, v101, v91
	v_mul_f32_e32 v84, v218, v84
	v_mul_f32_e32 v85, v219, v85
	v_mul_f32_e32 v86, v220, v86
	v_mul_f32_e32 v87, v221, v87
	v_mul_f32_e32 v88, v222, v88
	v_mul_f32_e32 v89, v223, v89
	v_mul_f32_e32 v90, v224, v90
	v_mul_f32_e32 v91, v225, v91
	v_cvt_pk_bf16_f32 v84, v84, v85
	v_cvt_pk_bf16_f32 v85, v86, v87
	v_cvt_pk_bf16_f32 v86, v88, v89
	v_cvt_pk_bf16_f32 v87, v90, v91
	ds_write_b128 v151, v[84:87] offset:8704
	ds_write_b128 v152, v[14:17] offset:8704
	v_lshlrev_b32_e32 v108, 16, v18
	v_and_b32_e32 v109, 0xffff0000, v18
	v_lshlrev_b32_e32 v110, 16, v19
	v_and_b32_e32 v111, 0xffff0000, v19
	v_lshlrev_b32_e32 v112, 16, v20
	v_and_b32_e32 v113, 0xffff0000, v20
	v_lshlrev_b32_e32 v114, 16, v21
	v_and_b32_e32 v115, 0xffff0000, v21
	v_mul_f32_e32 v108, v102, v108
	v_mul_f32_e32 v109, v102, v109
	v_mul_f32_e32 v110, v102, v110
	v_mul_f32_e32 v111, v102, v111
	v_mul_f32_e32 v112, v102, v112
	v_mul_f32_e32 v113, v102, v113
	v_mul_f32_e32 v114, v102, v114
	v_mul_f32_e32 v115, v102, v115
	v_mul_f32_e32 v108, v218, v108
	v_mul_f32_e32 v109, v219, v109
	v_mul_f32_e32 v110, v220, v110
	v_mul_f32_e32 v111, v221, v111
	v_mul_f32_e32 v112, v222, v112
	v_mul_f32_e32 v113, v223, v113
	v_mul_f32_e32 v114, v224, v114
	v_mul_f32_e32 v115, v225, v115
	v_cvt_pk_bf16_f32 v108, v108, v109
	v_cvt_pk_bf16_f32 v109, v110, v111
	v_cvt_pk_bf16_f32 v110, v112, v113
	v_cvt_pk_bf16_f32 v111, v114, v115
	ds_write_b128 v151, v[108:111] offset:17408
	ds_write_b128 v152, v[22:25] offset:17408
	v_lshlrev_b32_e32 v84, 16, v26
	v_and_b32_e32 v85, 0xffff0000, v26
	v_lshlrev_b32_e32 v86, 16, v27
	v_and_b32_e32 v87, 0xffff0000, v27
	v_lshlrev_b32_e32 v88, 16, v28
	v_and_b32_e32 v89, 0xffff0000, v28
	v_lshlrev_b32_e32 v90, 16, v29
	v_and_b32_e32 v91, 0xffff0000, v29
	v_mul_f32_e32 v84, v103, v84
	v_mul_f32_e32 v85, v103, v85
	v_mul_f32_e32 v86, v103, v86
	v_mul_f32_e32 v87, v103, v87
	v_mul_f32_e32 v88, v103, v88
	v_mul_f32_e32 v89, v103, v89
	v_mul_f32_e32 v90, v103, v90
	v_mul_f32_e32 v91, v103, v91
	v_mul_f32_e32 v84, v218, v84
	v_mul_f32_e32 v85, v219, v85
	v_mul_f32_e32 v86, v220, v86
	v_mul_f32_e32 v87, v221, v87
	v_mul_f32_e32 v88, v222, v88
	v_mul_f32_e32 v89, v223, v89
	v_mul_f32_e32 v90, v224, v90
	v_mul_f32_e32 v91, v225, v91
	v_cvt_pk_bf16_f32 v84, v84, v85
	v_cvt_pk_bf16_f32 v85, v86, v87
	v_cvt_pk_bf16_f32 v86, v88, v89
	v_cvt_pk_bf16_f32 v87, v90, v91
	ds_write_b128 v151, v[84:87] offset:26112
	ds_write_b128 v152, v[30:33] offset:26112
	v_lshlrev_b32_e32 v108, 16, v34
	v_and_b32_e32 v109, 0xffff0000, v34
	v_lshlrev_b32_e32 v110, 16, v35
	v_and_b32_e32 v111, 0xffff0000, v35
	v_lshlrev_b32_e32 v112, 16, v36
	v_and_b32_e32 v113, 0xffff0000, v36
	v_lshlrev_b32_e32 v114, 16, v37
	v_and_b32_e32 v115, 0xffff0000, v37
	v_mul_f32_e32 v108, v104, v108
	v_mul_f32_e32 v109, v104, v109
	v_mul_f32_e32 v110, v104, v110
	v_mul_f32_e32 v111, v104, v111
	v_mul_f32_e32 v112, v104, v112
	v_mul_f32_e32 v113, v104, v113
	v_mul_f32_e32 v114, v104, v114
	v_mul_f32_e32 v115, v104, v115
	v_mul_f32_e32 v108, v218, v108
	v_mul_f32_e32 v109, v219, v109
	v_mul_f32_e32 v110, v220, v110
	v_mul_f32_e32 v111, v221, v111
	v_mul_f32_e32 v112, v222, v112
	v_mul_f32_e32 v113, v223, v113
	v_mul_f32_e32 v114, v224, v114
	v_mul_f32_e32 v115, v225, v115
	v_cvt_pk_bf16_f32 v108, v108, v109
	v_cvt_pk_bf16_f32 v109, v110, v111
	v_cvt_pk_bf16_f32 v110, v112, v113
	v_cvt_pk_bf16_f32 v111, v114, v115
	ds_write_b128 v151, v[108:111] offset:34816
	ds_write_b128 v152, v[38:41] offset:34816
	v_lshlrev_b32_e32 v84, 16, v42
	v_and_b32_e32 v85, 0xffff0000, v42
	v_lshlrev_b32_e32 v86, 16, v43
	v_and_b32_e32 v87, 0xffff0000, v43
	v_lshlrev_b32_e32 v88, 16, v44
	v_and_b32_e32 v89, 0xffff0000, v44
	v_lshlrev_b32_e32 v90, 16, v45
	v_and_b32_e32 v91, 0xffff0000, v45
	v_mul_f32_e32 v84, v105, v84
	v_mul_f32_e32 v85, v105, v85
	v_mul_f32_e32 v86, v105, v86
	v_mul_f32_e32 v87, v105, v87
	v_mul_f32_e32 v88, v105, v88
	v_mul_f32_e32 v89, v105, v89
	v_mul_f32_e32 v90, v105, v90
	v_mul_f32_e32 v91, v105, v91
	v_mul_f32_e32 v84, v218, v84
	v_mul_f32_e32 v85, v219, v85
	v_mul_f32_e32 v86, v220, v86
	v_mul_f32_e32 v87, v221, v87
	v_mul_f32_e32 v88, v222, v88
	v_mul_f32_e32 v89, v223, v89
	v_mul_f32_e32 v90, v224, v90
	v_mul_f32_e32 v91, v225, v91
	v_cvt_pk_bf16_f32 v84, v84, v85
	v_cvt_pk_bf16_f32 v85, v86, v87
	v_cvt_pk_bf16_f32 v86, v88, v89
	v_cvt_pk_bf16_f32 v87, v90, v91
	ds_write_b128 v151, v[84:87] offset:43520
	ds_write_b128 v152, v[48:51] offset:43520
	v_lshlrev_b32_e32 v108, 16, v52
	v_and_b32_e32 v109, 0xffff0000, v52
	v_lshlrev_b32_e32 v110, 16, v53
	v_and_b32_e32 v111, 0xffff0000, v53
	v_lshlrev_b32_e32 v112, 16, v54
	v_and_b32_e32 v113, 0xffff0000, v54
	v_lshlrev_b32_e32 v114, 16, v55
	v_and_b32_e32 v115, 0xffff0000, v55
	v_mul_f32_e32 v108, v106, v108
	v_mul_f32_e32 v109, v106, v109
	v_mul_f32_e32 v110, v106, v110
	v_mul_f32_e32 v111, v106, v111
	v_mul_f32_e32 v112, v106, v112
	v_mul_f32_e32 v113, v106, v113
	v_mul_f32_e32 v114, v106, v114
	v_mul_f32_e32 v115, v106, v115
	v_mul_f32_e32 v108, v218, v108
	v_mul_f32_e32 v109, v219, v109
	v_mul_f32_e32 v110, v220, v110
	v_mul_f32_e32 v111, v221, v111
	v_mul_f32_e32 v112, v222, v112
	v_mul_f32_e32 v113, v223, v113
	v_mul_f32_e32 v114, v224, v114
	v_mul_f32_e32 v115, v225, v115
	v_cvt_pk_bf16_f32 v108, v108, v109
	v_cvt_pk_bf16_f32 v109, v110, v111
	v_cvt_pk_bf16_f32 v110, v112, v113
	v_cvt_pk_bf16_f32 v111, v114, v115
	ds_write_b128 v151, v[108:111] offset:52224
	ds_write_b128 v152, v[56:59] offset:52224
	v_lshlrev_b32_e32 v84, 16, v60
	v_and_b32_e32 v85, 0xffff0000, v60
	v_lshlrev_b32_e32 v86, 16, v61
	v_and_b32_e32 v87, 0xffff0000, v61
	v_lshlrev_b32_e32 v88, 16, v62
	v_and_b32_e32 v89, 0xffff0000, v62
	v_lshlrev_b32_e32 v90, 16, v63
	v_and_b32_e32 v91, 0xffff0000, v63
	v_mul_f32_e32 v84, v107, v84
	v_mul_f32_e32 v85, v107, v85
	v_mul_f32_e32 v86, v107, v86
	v_mul_f32_e32 v87, v107, v87
	v_mul_f32_e32 v88, v107, v88
	v_mul_f32_e32 v89, v107, v89
	v_mul_f32_e32 v90, v107, v90
	v_mul_f32_e32 v91, v107, v91
	v_mul_f32_e32 v84, v218, v84
	v_mul_f32_e32 v85, v219, v85
	v_mul_f32_e32 v86, v220, v86
	v_mul_f32_e32 v87, v221, v87
	v_mul_f32_e32 v88, v222, v88
	v_mul_f32_e32 v89, v223, v89
	v_mul_f32_e32 v90, v224, v90
	v_mul_f32_e32 v91, v225, v91
	v_cvt_pk_bf16_f32 v84, v84, v85
	v_cvt_pk_bf16_f32 v85, v86, v87
	v_cvt_pk_bf16_f32 v86, v88, v89
	v_cvt_pk_bf16_f32 v87, v90, v91
	ds_write_b128 v151, v[84:87] offset:60928
	ds_write_b128 v152, v[64:67] offset:60928
	v_lshlrev_b32_e32 v108, 16, v68
	v_and_b32_e32 v109, 0xffff0000, v68
	v_lshlrev_b32_e32 v84, 16, v72
	v_and_b32_e32 v85, 0xffff0000, v72
	v_lshlrev_b32_e32 v110, 16, v69
	v_and_b32_e32 v111, 0xffff0000, v69
	v_lshlrev_b32_e32 v86, 16, v73
	v_and_b32_e32 v87, 0xffff0000, v73
	v_lshlrev_b32_e32 v112, 16, v70
	v_and_b32_e32 v113, 0xffff0000, v70
	v_lshlrev_b32_e32 v88, 16, v74
	v_and_b32_e32 v89, 0xffff0000, v74
	v_lshlrev_b32_e32 v114, 16, v71
	v_and_b32_e32 v115, 0xffff0000, v71
	v_lshlrev_b32_e32 v90, 16, v75
	v_and_b32_e32 v91, 0xffff0000, v75
	v_mul_f32_e32 v116, v108, v108
	v_mul_f32_e32 v117, v84, v84
	v_fmac_f32_e32 v116, v109, v109
	v_fmac_f32_e32 v117, v85, v85
	v_fmac_f32_e32 v116, v110, v110
	v_fmac_f32_e32 v117, v86, v86
	v_fmac_f32_e32 v116, v111, v111
	v_fmac_f32_e32 v117, v87, v87
	v_fmac_f32_e32 v116, v112, v112
	v_fmac_f32_e32 v117, v88, v88
	v_fmac_f32_e32 v116, v113, v113
	v_fmac_f32_e32 v117, v89, v89
	v_fmac_f32_e32 v116, v114, v114
	v_fmac_f32_e32 v117, v90, v90
	v_fmac_f32_e32 v116, v115, v115
	v_fmac_f32_e32 v117, v91, v91
	v_lshlrev_b32_e32 v108, 16, v76
	v_and_b32_e32 v109, 0xffff0000, v76
	v_lshlrev_b32_e32 v84, 16, v80
	v_and_b32_e32 v85, 0xffff0000, v80
	v_lshlrev_b32_e32 v110, 16, v77
	v_and_b32_e32 v111, 0xffff0000, v77
	v_lshlrev_b32_e32 v86, 16, v81
	v_and_b32_e32 v87, 0xffff0000, v81
	v_lshlrev_b32_e32 v112, 16, v78
	v_and_b32_e32 v113, 0xffff0000, v78
	v_lshlrev_b32_e32 v88, 16, v82
	v_and_b32_e32 v89, 0xffff0000, v82
	v_lshlrev_b32_e32 v114, 16, v79
	v_and_b32_e32 v115, 0xffff0000, v79
	v_lshlrev_b32_e32 v90, 16, v83
	v_and_b32_e32 v91, 0xffff0000, v83
	v_mul_f32_e32 v118, v108, v108
	v_mul_f32_e32 v119, v84, v84
	v_fmac_f32_e32 v118, v109, v109
	v_fmac_f32_e32 v119, v85, v85
	v_fmac_f32_e32 v118, v110, v110
	v_fmac_f32_e32 v119, v86, v86
	v_fmac_f32_e32 v118, v111, v111
	v_fmac_f32_e32 v119, v87, v87
	v_fmac_f32_e32 v118, v112, v112
	v_fmac_f32_e32 v119, v88, v88
	v_fmac_f32_e32 v118, v113, v113
	v_fmac_f32_e32 v119, v89, v89
	v_fmac_f32_e32 v118, v114, v114
	v_fmac_f32_e32 v119, v90, v90
	v_fmac_f32_e32 v118, v115, v115
	v_fmac_f32_e32 v119, v91, v91
	v_add_f32_e32 v116, v116, v117
	v_add_f32_e32 v118, v118, v119
	v_add_f32_e32 v116, v116, v118
	ds_bpermute_b32 v117, v153, v116
	s_waitcnt lgkmcnt(0)
	v_add_f32_e32 v116, v116, v117
	ds_bpermute_b32 v117, v154, v116
	s_waitcnt lgkmcnt(0)
	v_add_f32_e32 v116, v116, v117
	v_fmamk_f32 v116, v116, 0x3c000000, v198
	v_rsq_f32_e32 v116, v116
	s_add_i32 s43, s42, s52
	s_cmpk_gt_i32 s43, 0x5ff
	v_mul_f32_e32 v116, 0x3db504f3, v116
	v_lshlrev_b32_e32 v108, 16, v68
	v_and_b32_e32 v109, 0xffff0000, v68
	v_lshlrev_b32_e32 v110, 16, v69
	v_and_b32_e32 v111, 0xffff0000, v69
	v_lshlrev_b32_e32 v112, 16, v70
	v_and_b32_e32 v113, 0xffff0000, v70
	v_lshlrev_b32_e32 v114, 16, v71
	v_and_b32_e32 v115, 0xffff0000, v71
	v_mul_f32_e32 v108, v116, v108
	v_mul_f32_e32 v109, v116, v109
	v_mul_f32_e32 v110, v116, v110
	v_mul_f32_e32 v111, v116, v111
	v_mul_f32_e32 v112, v116, v112
	v_mul_f32_e32 v113, v116, v113
	v_mul_f32_e32 v114, v116, v114
	v_mul_f32_e32 v115, v116, v115
	v_mul_f32_e32 v108, v108, v226
	v_mul_f32_e32 v109, v109, v227
	v_mul_f32_e32 v110, v110, v228
	v_mul_f32_e32 v111, v111, v229
	v_mul_f32_e32 v112, v112, v230
	v_mul_f32_e32 v113, v113, v231
	v_mul_f32_e32 v114, v114, v232
	v_mul_f32_e32 v115, v115, v233
	v_cvt_pk_bf16_f32 v84, v108, v109
	v_cvt_pk_bf16_f32 v85, v110, v111
	v_cvt_pk_bf16_f32 v86, v112, v113
	v_cvt_pk_bf16_f32 v87, v114, v115
	v_lshlrev_b32_e32 v108, 16, v72
	v_and_b32_e32 v109, 0xffff0000, v72
	v_lshlrev_b32_e32 v110, 16, v73
	v_and_b32_e32 v111, 0xffff0000, v73
	v_lshlrev_b32_e32 v112, 16, v74
	v_and_b32_e32 v113, 0xffff0000, v74
	v_lshlrev_b32_e32 v114, 16, v75
	v_and_b32_e32 v115, 0xffff0000, v75
	v_mul_f32_e32 v108, v116, v108
	v_mul_f32_e32 v109, v116, v109
	v_mul_f32_e32 v110, v116, v110
	v_mul_f32_e32 v111, v116, v111
	v_mul_f32_e32 v112, v116, v112
	v_mul_f32_e32 v113, v116, v113
	v_mul_f32_e32 v114, v116, v114
	v_mul_f32_e32 v115, v116, v115
	v_mul_f32_e32 v108, v108, v234
	v_mul_f32_e32 v109, v109, v235
	v_mul_f32_e32 v110, v110, v236
	v_mul_f32_e32 v111, v111, v237
	v_mul_f32_e32 v112, v112, v238
	v_mul_f32_e32 v113, v113, v239
	v_mul_f32_e32 v114, v114, v240
	v_mul_f32_e32 v115, v115, v241
	v_cvt_pk_bf16_f32 v88, v108, v109
	v_cvt_pk_bf16_f32 v89, v110, v111
	v_cvt_pk_bf16_f32 v90, v112, v113
	v_cvt_pk_bf16_f32 v91, v114, v115
	v_lshlrev_b32_e32 v108, 16, v76
	v_and_b32_e32 v109, 0xffff0000, v76
	v_lshlrev_b32_e32 v110, 16, v77
	v_and_b32_e32 v111, 0xffff0000, v77
	v_lshlrev_b32_e32 v112, 16, v78
	v_and_b32_e32 v113, 0xffff0000, v78
	v_lshlrev_b32_e32 v114, 16, v79
	v_and_b32_e32 v115, 0xffff0000, v79
	v_mul_f32_e32 v108, v116, v108
	v_mul_f32_e32 v109, v116, v109
	v_mul_f32_e32 v110, v116, v110
	v_mul_f32_e32 v111, v116, v111
	v_mul_f32_e32 v112, v116, v112
	v_mul_f32_e32 v113, v116, v113
	v_mul_f32_e32 v114, v116, v114
	v_mul_f32_e32 v115, v116, v115
	v_mul_f32_e32 v108, v108, v242
	v_mul_f32_e32 v109, v109, v243
	v_mul_f32_e32 v110, v110, v244
	v_mul_f32_e32 v111, v111, v245
	v_mul_f32_e32 v112, v112, v246
	v_mul_f32_e32 v113, v113, v247
	v_mul_f32_e32 v114, v114, v248
	v_mul_f32_e32 v115, v115, v249
	v_cvt_pk_bf16_f32 v92, v108, v109
	v_cvt_pk_bf16_f32 v93, v110, v111
	v_cvt_pk_bf16_f32 v94, v112, v113
	v_cvt_pk_bf16_f32 v95, v114, v115
	v_lshlrev_b32_e32 v108, 16, v80
	v_and_b32_e32 v109, 0xffff0000, v80
	v_lshlrev_b32_e32 v110, 16, v81
	v_and_b32_e32 v111, 0xffff0000, v81
	v_lshlrev_b32_e32 v112, 16, v82
	v_and_b32_e32 v113, 0xffff0000, v82
	v_lshlrev_b32_e32 v114, 16, v83
	v_and_b32_e32 v115, 0xffff0000, v83
	v_mul_f32_e32 v108, v116, v108
	v_mul_f32_e32 v109, v116, v109
	v_mul_f32_e32 v110, v116, v110
	v_mul_f32_e32 v111, v116, v111
	v_mul_f32_e32 v112, v116, v112
	v_mul_f32_e32 v113, v116, v113
	v_mul_f32_e32 v114, v116, v114
	v_mul_f32_e32 v115, v116, v115
	v_mul_f32_e32 v108, v108, v250
	v_mul_f32_e32 v109, v109, v251
	v_mul_f32_e32 v110, v110, v252
	v_mul_f32_e32 v111, v111, v253
	v_mul_f32_e32 v112, v112, v120
	v_mul_f32_e32 v113, v113, v121
	v_mul_f32_e32 v114, v114, v122
	v_mul_f32_e32 v115, v115, v123
	v_cvt_pk_bf16_f32 v96, v108, v109
	v_cvt_pk_bf16_f32 v97, v110, v111
	v_cvt_pk_bf16_f32 v98, v112, v113
	v_cvt_pk_bf16_f32 v99, v114, v115
	s_cselect_b64 s[34:35], -1, 0
	s_and_b64 vcc, exec, s[34:35]
	s_waitcnt lgkmcnt(0)
	s_barrier
	s_cbranch_vccnz .LBB0_725
	s_ashr_i32 s10, s43, 9
	s_lshl_b32 s44, s10, 1
	s_lshr_b32 s37, 64, s44
	s_and_b32 s36, s43, 63
	s_sub_i32 s45, 6, s44
	s_add_i32 s37, s37, -1
	s_bfe_u32 s11, s43, 0x30006
	s_lshr_b32 s45, s36, s45
	s_and_b32 s36, s37, s36
	s_lshl_b32 s10, s10, 3
	s_or_b32 s47, s10, s11
	s_lshl_b32 s46, s36, 7
	s_cmp_lg_u32 s36, 0
	s_cselect_b64 s[10:11], -1, 0
	s_cmp_eq_u32 s36, 0
	v_or_b32_e32 v60, s46, v1
	s_cbranch_scc1 .LBB0_807
	v_add_u32_e32 v2, 0xffffff80, v60
	v_lshlrev_b32_e32 v2, s44, v2
	v_add_u32_e32 v2, s45, v2
	v_mul_lo_u32 v2, v2, s38
	v_lshl_add_u32 v2, s47, 7, v2
	v_or_b32_e32 v2, v2, v143
	v_mov_b32_e32 v3, v46
	v_lshl_add_u64 v[2:3], v[2:3], 1, s[18:19]
	v_add_co_u32_e32 v4, vcc, 0x1000, v2
	s_nop 1
	v_addc_co_u32_e32 v5, vcc, 0, v3, vcc
	v_add_co_u32_e32 v6, vcc, 0x3000, v2
	s_nop 1
	v_addc_co_u32_e32 v7, vcc, 0, v3, vcc
	global_load_dwordx4 v[2:5], v[4:5], off offset:2048
	s_nop 0
	global_load_dwordx4 v[6:9], v[6:7], off
	s_cbranch_execnz .LBB0_715
